# prologue even in-projection weight conversion: 32 serialised predicated loads per item issued up front
# speedup vs baseline: 1.0164x; 1.0029x over previous
; #define LDS_WAIT() asm volatile("s_waitcnt lgkmcnt(0)" ::: "memory")
; __device__ __forceinline__ void p0_prologue(const Args& a, const int wv) {
;     ...
;             if (it < T0) { const int m = it / I_WINE, r = it % I_WINE, kb = r / 78, nb = r % 78;
;                 const float* W = a.hy_w_in + (size_t)m * DM * EVEN_IN; bf16_t* WT = (bf16_t*)(ws + WS_WINE) + (size_t)m * EVEN_INP * DM;
;                 const int k0 = 64 * kb, n0 = 32 * nb; const RmWinE rm;
; #pragma unroll 8
;                 for (int i = 0; i < 32; ++i) { const int kk = 2 * i + (F.lane >> 5), n = n0 + (F.lane & 31); scr[kk * 33 + (F.lane & 31)] = (n < EVEN_IN) ? W[(size_t)(k0 + kk) * EVEN_IN + n] : 0.f; }
;                 LDS_WAIT(); asm volatile("" ::: "memory");
.LBB0_59:
	s_mul_hi_i32 s2, s12, 0xd20d20d3
	s_add_i32 s2, s2, s12
	s_lshr_b32 s6, s2, 31
	s_ashr_i32 s2, s2, 10
	s_add_i32 s10, s2, s6
	s_mul_i32 s2, s10, 0x4e0
	s_sub_i32 s2, s12, s2
	s_mul_i32 s6, s2, 0x6907
	s_lshr_b32 s7, s6, 31
	s_ashr_i32 s11, s6, 21
	s_add_i32 s11, s11, s7
	s_mul_i32 s6, s11, 0x4e
	s_sub_i32 s2, s2, s6
	s_load_dwordx2 s[6:7], s[4:5], 0x38
	s_sext_i32_i16 s2, s2
	s_lshl_b32 s2, s2, 5
	s_mul_i32 s90, s11, 0x26c00
	s_mul_i32 s9, s10, 0x9b0000
	v_or_b32_e32 v0, s2, v151
	s_add_i32 s90, s2, s90
	s_mul_hi_i32 s8, s10, 0x9b0000
	v_cmp_gt_i32_e32 vcc, s37, v0
	v_add_u32_e32 v0, s90, v190
	s_waitcnt lgkmcnt(0)
	s_add_u32 s6, s6, s9
	v_add_u32_e32 v2, s90, v191
	v_add_u32_e32 v4, s90, v192
	v_add_u32_e32 v6, s90, v193
	v_add_u32_e32 v8, s90, v194
	v_add_u32_e32 v10, s90, v195
	v_add_u32_e32 v12, s90, v196
	v_add_u32_e32 v14, s90, v189
	v_ashrrev_i32_e32 v1, 31, v0
	s_addc_u32 s7, s7, s8
	v_ashrrev_i32_e32 v3, 31, v2
	v_ashrrev_i32_e32 v5, 31, v4
	v_ashrrev_i32_e32 v7, 31, v6
	v_ashrrev_i32_e32 v9, 31, v8
	v_ashrrev_i32_e32 v11, 31, v10
	v_ashrrev_i32_e32 v13, 31, v12
	v_ashrrev_i32_e32 v15, 31, v14
	v_lshl_add_u64 v[0:1], v[0:1], 2, s[6:7]
	v_lshl_add_u64 v[2:3], v[2:3], 2, s[6:7]
	v_lshl_add_u64 v[4:5], v[4:5], 2, s[6:7]
	v_lshl_add_u64 v[6:7], v[6:7], 2, s[6:7]
	v_lshl_add_u64 v[8:9], v[8:9], 2, s[6:7]
	v_lshl_add_u64 v[10:11], v[10:11], 2, s[6:7]
	v_lshl_add_u64 v[12:13], v[12:13], 2, s[6:7]
	v_lshl_add_u64 v[14:15], v[14:15], 2, s[6:7]
	s_mov_b64 s[6:7], 0
	v_mov_b32_e32 v16, v187
	v_mov_b32_e32 v20, 0
	v_mov_b32_e32 v21, 0
	v_mov_b32_e32 v22, 0
	v_mov_b32_e32 v23, 0
	v_mov_b32_e32 v24, 0
	v_mov_b32_e32 v25, 0
	v_mov_b32_e32 v26, 0
	v_mov_b32_e32 v27, 0
	v_mov_b32_e32 v28, 0
	v_mov_b32_e32 v29, 0
	v_mov_b32_e32 v30, 0
	v_mov_b32_e32 v31, 0
	v_mov_b32_e32 v32, 0
	v_mov_b32_e32 v33, 0
	v_mov_b32_e32 v34, 0
	v_mov_b32_e32 v35, 0
	v_mov_b32_e32 v36, 0
	v_mov_b32_e32 v37, 0
	v_mov_b32_e32 v38, 0
	v_mov_b32_e32 v39, 0
	v_mov_b32_e32 v40, 0
	v_mov_b32_e32 v41, 0
	v_mov_b32_e32 v42, 0
	v_mov_b32_e32 v43, 0
	v_mov_b32_e32 v44, 0
	v_mov_b32_e32 v45, 0
	v_mov_b32_e32 v46, 0
	v_mov_b32_e32 v47, 0
	v_mov_b32_e32 v48, 0
	v_mov_b32_e32 v49, 0
	v_mov_b32_e32 v50, 0
	v_mov_b32_e32 v51, 0
	s_and_saveexec_b64 s[8:9], vcc
	v_lshl_add_u64 v[18:19], v[14:15], 0, s[6:7]
	global_load_dword v20, v[18:19], off
	v_lshl_add_u64 v[18:19], v[12:13], 0, s[6:7]
	global_load_dword v21, v[18:19], off
	v_lshl_add_u64 v[18:19], v[10:11], 0, s[6:7]
	global_load_dword v22, v[18:19], off
	v_lshl_add_u64 v[18:19], v[8:9], 0, s[6:7]
	global_load_dword v23, v[18:19], off
	v_lshl_add_u64 v[18:19], v[6:7], 0, s[6:7]
	global_load_dword v24, v[18:19], off
	v_lshl_add_u64 v[18:19], v[4:5], 0, s[6:7]
	global_load_dword v25, v[18:19], off
	v_lshl_add_u64 v[18:19], v[2:3], 0, s[6:7]
	global_load_dword v26, v[18:19], off
	v_lshl_add_u64 v[18:19], v[0:1], 0, s[6:7]
	global_load_dword v27, v[18:19], off
	s_add_u32 s6, s6, 0x26c00
	s_addc_u32 s7, s7, 0
	v_lshl_add_u64 v[18:19], v[14:15], 0, s[6:7]
	global_load_dword v28, v[18:19], off
	v_lshl_add_u64 v[18:19], v[12:13], 0, s[6:7]
	global_load_dword v29, v[18:19], off
	v_lshl_add_u64 v[18:19], v[10:11], 0, s[6:7]
	global_load_dword v30, v[18:19], off
	v_lshl_add_u64 v[18:19], v[8:9], 0, s[6:7]
	global_load_dword v31, v[18:19], off
	v_lshl_add_u64 v[18:19], v[6:7], 0, s[6:7]
	global_load_dword v32, v[18:19], off
	v_lshl_add_u64 v[18:19], v[4:5], 0, s[6:7]
	global_load_dword v33, v[18:19], off
	v_lshl_add_u64 v[18:19], v[2:3], 0, s[6:7]
	global_load_dword v34, v[18:19], off
	v_lshl_add_u64 v[18:19], v[0:1], 0, s[6:7]
	global_load_dword v35, v[18:19], off
	s_add_u32 s6, s6, 0x26c00
	s_addc_u32 s7, s7, 0
	v_lshl_add_u64 v[18:19], v[14:15], 0, s[6:7]
	global_load_dword v36, v[18:19], off
	v_lshl_add_u64 v[18:19], v[12:13], 0, s[6:7]
	global_load_dword v37, v[18:19], off
	v_lshl_add_u64 v[18:19], v[10:11], 0, s[6:7]
	global_load_dword v38, v[18:19], off
	v_lshl_add_u64 v[18:19], v[8:9], 0, s[6:7]
	global_load_dword v39, v[18:19], off
	v_lshl_add_u64 v[18:19], v[6:7], 0, s[6:7]
	global_load_dword v40, v[18:19], off
	v_lshl_add_u64 v[18:19], v[4:5], 0, s[6:7]
	global_load_dword v41, v[18:19], off
	v_lshl_add_u64 v[18:19], v[2:3], 0, s[6:7]
	global_load_dword v42, v[18:19], off
	v_lshl_add_u64 v[18:19], v[0:1], 0, s[6:7]
	global_load_dword v43, v[18:19], off
	s_add_u32 s6, s6, 0x26c00
	s_addc_u32 s7, s7, 0
	v_lshl_add_u64 v[18:19], v[14:15], 0, s[6:7]
	global_load_dword v44, v[18:19], off
	v_lshl_add_u64 v[18:19], v[12:13], 0, s[6:7]
	global_load_dword v45, v[18:19], off
	v_lshl_add_u64 v[18:19], v[10:11], 0, s[6:7]
	global_load_dword v46, v[18:19], off
	v_lshl_add_u64 v[18:19], v[8:9], 0, s[6:7]
	global_load_dword v47, v[18:19], off
	v_lshl_add_u64 v[18:19], v[6:7], 0, s[6:7]
	global_load_dword v48, v[18:19], off
	v_lshl_add_u64 v[18:19], v[4:5], 0, s[6:7]
	global_load_dword v49, v[18:19], off
	v_lshl_add_u64 v[18:19], v[2:3], 0, s[6:7]
	global_load_dword v50, v[18:19], off
	v_lshl_add_u64 v[18:19], v[0:1], 0, s[6:7]
	global_load_dword v51, v[18:19], off
	s_add_u32 s6, s6, 0x26c00
	s_addc_u32 s7, s7, 0
	s_or_b64 exec, exec, s[8:9]
	s_waitcnt vmcnt(31)
	ds_write_b32 v16, v20
	s_waitcnt vmcnt(30)
	ds_write_b32 v16, v21 offset:264
	s_waitcnt vmcnt(29)
	ds_write_b32 v16, v22 offset:528
	s_waitcnt vmcnt(28)
	ds_write_b32 v16, v23 offset:792
	s_waitcnt vmcnt(27)
	ds_write_b32 v16, v24 offset:1056
	s_waitcnt vmcnt(26)
	ds_write_b32 v16, v25 offset:1320
	s_waitcnt vmcnt(25)
	ds_write_b32 v16, v26 offset:1584
	s_waitcnt vmcnt(24)
	ds_write_b32 v16, v27 offset:1848
	s_waitcnt vmcnt(23)
	ds_write_b32 v16, v28 offset:2112
	s_waitcnt vmcnt(22)
	ds_write_b32 v16, v29 offset:2376
	s_waitcnt vmcnt(21)
	ds_write_b32 v16, v30 offset:2640
	s_waitcnt vmcnt(20)
	ds_write_b32 v16, v31 offset:2904
	s_waitcnt vmcnt(19)
	ds_write_b32 v16, v32 offset:3168
	s_waitcnt vmcnt(18)
	ds_write_b32 v16, v33 offset:3432
	s_waitcnt vmcnt(17)
	ds_write_b32 v16, v34 offset:3696
	s_waitcnt vmcnt(16)
	ds_write_b32 v16, v35 offset:3960
	s_waitcnt vmcnt(15)
	ds_write_b32 v16, v36 offset:4224
	s_waitcnt vmcnt(14)
	ds_write_b32 v16, v37 offset:4488
	s_waitcnt vmcnt(13)
	ds_write_b32 v16, v38 offset:4752
	s_waitcnt vmcnt(12)
	ds_write_b32 v16, v39 offset:5016
	s_waitcnt vmcnt(11)
	ds_write_b32 v16, v40 offset:5280
	s_waitcnt vmcnt(10)
	ds_write_b32 v16, v41 offset:5544
	s_waitcnt vmcnt(9)
	ds_write_b32 v16, v42 offset:5808
	s_waitcnt vmcnt(8)
	ds_write_b32 v16, v43 offset:6072
	s_waitcnt vmcnt(7)
	ds_write_b32 v16, v44 offset:6336
	s_waitcnt vmcnt(6)
	ds_write_b32 v16, v45 offset:6600
	s_waitcnt vmcnt(5)
	ds_write_b32 v16, v46 offset:6864
	s_waitcnt vmcnt(4)
	ds_write_b32 v16, v47 offset:7128
	s_waitcnt vmcnt(3)
	ds_write_b32 v16, v48 offset:7392
	s_waitcnt vmcnt(2)
	ds_write_b32 v16, v49 offset:7656
	s_waitcnt vmcnt(1)
	ds_write_b32 v16, v50 offset:7920
	s_waitcnt vmcnt(0)
	ds_write_b32 v16, v51 offset:8184
	v_add_u32_e32 v16, 0x2100, v16
